# baseline (speedup 1.0000x reference)
_Z9fast_mainILb0EEvPKiS1_S1_PKfPKcS3_PfS6_PiPyS6_:
	s_load_dwordx4 s[4:7], s[0:1], 0x20
	s_load_dwordx4 s[8:11], s[0:1], 0x8
	s_load_dwordx2 s[16:17], s[0:1], 0x0
	v_and_b32_e32 v1, 63, v0
	v_lshrrev_b32_e32 v8, 6, v0
	v_lshlrev_b32_e32 v150, 4, v1
	v_lshl_or_b32 v14, s2, 3, v8
	v_lshlrev_b32_e32 v14, 10, v14
	v_or_b32_e32 v14, v14, v150
	v_add_u32_e32 v212, 0x10000, v150
	v_add_u32_e32 v213, 0x18c00, v150
	v_mov_b32_e32 v151, 0
	s_waitcnt lgkmcnt(0)
	global_load_dwordx4 v[20:23], v14, s[16:17]
	v_lshl_add_u64 v[4:5], s[4:5], 0, v[150:151]
	v_lshlrev_b32_e32 v2, 10, v8
	v_mov_b32_e32 v3, v151
	v_lshl_add_u64 v[6:7], v[4:5], 0, v[2:3]
	v_readfirstlane_b32 s3, v2
	v_or_b32_e32 v3, 0x2000, v2
	s_mov_b32 m0, s3
	s_mov_b64 s[4:5], 0x2000
	v_readfirstlane_b32 s3, v3
	global_load_lds_dwordx4 v[6:7], off
	v_lshl_add_u64 v[10:11], v[6:7], 0, s[4:5]
	s_mov_b32 m0, s3
	v_or_b32_e32 v3, 0x6000, v2
	global_load_lds_dwordx4 v[10:11], off
	v_or_b32_e32 v10, 0x4000, v2
	v_mov_b32_e32 v11, v151
	v_readfirstlane_b32 s3, v10
	v_lshl_add_u64 v[12:13], v[4:5], 0, v[10:11]
	s_mov_b32 m0, s3
	s_mov_b64 s[4:5], 0x6000
	v_readfirstlane_b32 s3, v3
	global_load_lds_dwordx4 v[12:13], off
	v_lshl_add_u64 v[10:11], v[6:7], 0, s[4:5]
	s_mov_b32 m0, s3
	v_or_b32_e32 v3, 0xa000, v2
	global_load_lds_dwordx4 v[10:11], off
	v_or_b32_e32 v10, 0x8000, v2
	v_mov_b32_e32 v11, v151
	v_readfirstlane_b32 s3, v10
	v_lshl_add_u64 v[12:13], v[4:5], 0, v[10:11]
	s_mov_b32 m0, s3
	s_mov_b64 s[4:5], 0xa000
	v_readfirstlane_b32 s3, v3
	global_load_lds_dwordx4 v[12:13], off
	v_lshl_add_u64 v[10:11], v[6:7], 0, s[4:5]
	s_mov_b32 m0, s3
	v_or_b32_e32 v3, 0xe000, v2
	global_load_lds_dwordx4 v[10:11], off
	v_or_b32_e32 v10, 0xc000, v2
	v_mov_b32_e32 v11, v151
	v_readfirstlane_b32 s3, v10
	v_lshl_add_u64 v[12:13], v[4:5], 0, v[10:11]
	s_mov_b32 m0, s3
	s_mov_b64 s[4:5], 0xe000
	v_readfirstlane_b32 s3, v3
	global_load_lds_dwordx4 v[12:13], off
	v_lshl_add_u64 v[10:11], v[6:7], 0, s[4:5]
	s_mov_b32 m0, s3
	v_or_b32_e32 v3, 0x12000, v2
	global_load_lds_dwordx4 v[10:11], off
	v_or_b32_e32 v10, 0x10000, v2
	v_mov_b32_e32 v11, v151
	v_readfirstlane_b32 s3, v10
	v_lshl_add_u64 v[12:13], v[4:5], 0, v[10:11]
	s_mov_b32 m0, s3
	s_mov_b64 s[4:5], 0x12000
	v_readfirstlane_b32 s3, v3
	global_load_lds_dwordx4 v[12:13], off
	v_lshl_add_u64 v[10:11], v[6:7], 0, s[4:5]
	s_mov_b32 m0, s3
	s_nop 0
	global_load_lds_dwordx4 v[10:11], off
	v_or_b32_e32 v10, 0x14000, v2
	v_mov_b32_e32 v11, v151
	v_readfirstlane_b32 s3, v10
	v_lshl_add_u64 v[12:13], v[4:5], 0, v[10:11]
	s_mov_b32 m0, s3
	s_movk_i32 s3, 0x2c0
	global_load_lds_dwordx4 v[12:13], off
	v_cmp_gt_u32_e32 vcc, s3, v0
	s_and_saveexec_b64 s[4:5], vcc
	s_cbranch_execz .LBB1_2
	v_or_b32_e32 v3, 0x16000, v2
	s_mov_b64 s[12:13], 0x16000
	v_readfirstlane_b32 s3, v3
	v_lshl_add_u64 v[6:7], v[6:7], 0, s[12:13]
	s_mov_b32 m0, s3
	s_nop 0
	global_load_lds_dwordx4 v[6:7], off
.LBB1_2:
	s_or_b64 exec, exec, s[4:5]
	v_or_b32_e32 v3, 0x60, v8
	s_movk_i32 s3, 0x63
	v_cmp_gt_u32_e32 vcc, s3, v3
	s_and_saveexec_b64 s[12:13], vcc
	s_cbranch_execz .LBB1_4
	v_lshlrev_b32_e32 v6, 10, v3
	v_mov_b32_e32 v7, 0
	v_readfirstlane_b32 s3, v6
	v_lshl_add_u64 v[4:5], v[4:5], 0, v[6:7]
	s_mov_b32 m0, s3
	s_nop 0
	global_load_lds_dwordx4 v[4:5], off
.LBB1_4:
	s_or_b64 exec, exec, s[12:13]
	v_lshl_or_b32 v8, s2, 3, v8
	v_mov_b32_e32 v151, 0
	v_readfirstlane_b32 s4, v8
	s_ashr_i32 s5, s4, 31
	s_lshl_b64 s[4:5], s[4:5], 2
	s_add_u32 s8, s8, s4
	v_add_u32_e32 v172, 0x22c00, v2
	s_addc_u32 s9, s9, s5
	v_lshl_add_u32 v173, v1, 2, v172
	s_add_u32 s4, s10, s4
	ds_write_b32 v173, v151
	s_addc_u32 s5, s11, s5
	s_load_dword s12, s[6:7], 0x4000
	v_mov_b32_e32 v2, 1
	s_load_dword s8, s[8:9], 0x0
	v_lshrrev_b32_e32 v18, 5, v1
	s_load_dword s3, s[4:5], 0x0
	s_waitcnt lgkmcnt(0)
	s_movk_i32 s4, 0xff
	v_cmp_lt_u32_e32 vcc, s4, v0
	v_bfe_u32 v64, v0, 6, 1
	v_lshlrev_b32_e32 v174, 4, v18
	s_waitcnt vmcnt(12)
	v_lshl_add_u32 v3, v20, 2, v172
	v_lshl_add_u32 v4, v21, 2, v172
	v_lshl_add_u32 v5, v22, 2, v172
	v_lshl_add_u32 v6, v23, 2, v172
	ds_add_u32 v3, v2
	ds_add_u32 v4, v2
	ds_add_u32 v5, v2
	ds_add_u32 v6, v2
	s_waitcnt lgkmcnt(0)
	ds_read_b32 v151, v173
	s_waitcnt lgkmcnt(0)
	v_lshl_or_b32 v2, s8, 6, v1
	v_ashrrev_i32_e32 v3, 31, v2
	v_lshl_add_u64 v[2:3], v[2:3], 2, s[6:7]
	v_cvt_f32_i32_e32 v4, v151
	ds_write_b32 v173, v4 offset:256
	s_waitcnt vmcnt(7)
	s_waitcnt lgkmcnt(0)
	s_barrier
	global_load_dword v175, v[2:3], off
	s_and_saveexec_b64 s[4:5], vcc
	s_xor_b64 s[4:5], exec, s[4:5]
	s_cbranch_execz .LBB1_6
	v_lshlrev_b32_e32 v2, 2, v0
	v_and_b32_e32 v2, 0x7c, v2
	v_bfe_u32 v19, v0, 7, 1
	v_lshl_or_b32 v2, v64, 7, v2
	v_lshl_or_b32 v32, v19, 12, v150
	ds_read_b32 v2, v2 offset:35584
	ds_read_b128 v[20:23], v32
	v_lshlrev_b32_e32 v40, 12, v64
	v_or_b32_e32 v41, v40, v150
	ds_read_b128 v[24:27], v41 offset:24576
	ds_read_b128 v[28:31], v32 offset:3072
	s_waitcnt lgkmcnt(3)
	v_mov_b32_e32 v3, v2
	v_mov_b32_e32 v4, v2
	v_mov_b32_e32 v5, v2
	v_mov_b32_e32 v6, v2
	v_mov_b32_e32 v7, v2
	v_mov_b32_e32 v8, v2
	v_mov_b32_e32 v9, v2
	v_mov_b32_e32 v10, v2
	v_mov_b32_e32 v11, v2
	v_mov_b32_e32 v12, v2
	v_mov_b32_e32 v13, v2
	v_mov_b32_e32 v14, v2
	v_mov_b32_e32 v15, v2
	v_mov_b32_e32 v16, v2
	v_mov_b32_e32 v17, v2
	v_lshlrev_b32_e32 v19, 11, v19
	v_or3_b32 v19, v19, v40, v150
	s_waitcnt lgkmcnt(1)
	v_mfma_f32_32x32x16_bf16 v[2:17], v[20:23], v[24:27], v[2:17]
	ds_read_b128 v[20:23], v32 offset:1024
	ds_read_b128 v[24:27], v41 offset:25600
	ds_read_b128 v[32:35], v32 offset:2048
	ds_read_b128 v[36:39], v41 offset:26624
	v_add_u32_e32 v19, 0x20c00, v19
	s_waitcnt lgkmcnt(2)
	v_mfma_f32_32x32x16_bf16 v[2:17], v[20:23], v[24:27], v[2:17]
	ds_read_b128 v[20:23], v41 offset:27648
	s_waitcnt lgkmcnt(1)
	v_mfma_f32_32x32x16_bf16 v[2:17], v[32:35], v[36:39], v[2:17]
	s_waitcnt lgkmcnt(0)
	v_mfma_f32_32x32x16_bf16 v[2:17], v[28:31], v[20:23], v[2:17]
	s_nop 11
	v_cvt_pk_bf16_f32 v9, v8, v9
	v_cvt_pk_bf16_f32 v8, v6, v7
	v_cvt_pk_bf16_f32 v7, v4, v5
	v_cvt_pk_bf16_f32 v6, v2, v3
	v_cvt_pk_bf16_f32 v5, v16, v17
	v_cvt_pk_bf16_f32 v4, v14, v15
	v_cvt_pk_bf16_f32 v3, v12, v13
	v_cvt_pk_bf16_f32 v2, v10, v11
	ds_write_b128 v19, v[6:9]
	ds_write_b128 v19, v[2:5] offset:1024
	v_lshlrev_b32_e32 v2, 4, v18

.LBB1_8:
	s_or_b64 exec, exec, s[4:5]
	v_add_u32_e32 v10, v172, v2
	s_waitcnt vmcnt(1) lgkmcnt(0)
	s_barrier
	ds_read_b128 v[18:21], v10 offset:256
	ds_read_b128 v[22:25], v10 offset:288
	ds_read_b128 v[82:85], v10 offset:320
	ds_read_b128 v[86:89], v10 offset:352
	ds_read_b128 v[74:77], v10 offset:384
	ds_read_b128 v[78:81], v10 offset:416
	ds_read_b128 v[2:5], v213 offset:32768
	ds_read_b128 v[6:9], v213 offset:0
	ds_read_b128 v[66:69], v10 offset:448
	ds_read_b128 v[70:73], v10 offset:480
	ds_read_b128 v[10:13], v213 offset:1024
	s_waitcnt lgkmcnt(3)
	v_pk_mul_f32 v[26:27], v[8:9], v[20:21]
	v_pk_mul_f32 v[28:29], v[6:7], v[18:19]
	ds_read_b128 v[14:17], v213 offset:8192
	s_waitcnt lgkmcnt(1)
	v_pk_mul_f32 v[12:13], v[12:13], v[24:25]
	v_pk_mul_f32 v[10:11], v[10:11], v[22:23]
	v_pk_fma_f32 v[30:31], v[8:9], v[20:21], v[12:13]
	v_pk_fma_f32 v[32:33], v[6:7], v[18:19], v[10:11]
	v_cvt_pk_bf16_f32 v9, v12, v13
	v_cvt_pk_bf16_f32 v7, v26, v27
	v_cvt_pk_bf16_f32 v8, v10, v11
	v_cvt_pk_bf16_f32 v6, v28, v29
	ds_read_b128 v[10:13], v213 offset:33792
	s_nop 0
	v_mfma_f32_32x32x16_bf16 v[34:49], v[2:5], v[6:9], 0
	ds_read_b128 v[6:9], v213 offset:9216
	s_waitcnt lgkmcnt(2)
	v_mul_f32_e64 v26, v16, v20
	v_mul_f32_e64 v27, v17, v21
	v_pk_mul_f32 v[50:51], v[14:15], v[18:19]
	s_mov_b32 s4, 0x3727c5ac
	s_waitcnt lgkmcnt(0)
	v_pk_mul_f32 v[8:9], v[8:9], v[24:25]
	v_pk_mul_f32 v[28:29], v[6:7], v[22:23]
	v_pk_fma_f32 v[90:91], v[16:17], v[20:21], v[8:9]
	v_pk_fma_f32 v[92:93], v[14:15], v[18:19], v[28:29]
	ds_read_b128 v[14:17], v213 offset:2048
	v_cvt_pk_bf16_f32 v9, v8, v9
	v_cvt_pk_bf16_f32 v7, v26, v27
	v_cvt_pk_bf16_f32 v8, v28, v29
	ds_read_b128 v[26:29], v213 offset:3072
	v_cvt_pk_bf16_f32 v6, v50, v51
	s_waitcnt lgkmcnt(1)
	v_pk_mul_f32 v[94:95], v[14:15], v[82:83]
	s_mov_b32 s0, 0x3c800000
	v_mfma_f32_32x32x16_bf16 v[50:65], v[2:5], v[6:9], 0
	v_mul_f32_e64 v2, v16, v84
	v_mul_f32_e64 v3, v17, v85
	s_waitcnt lgkmcnt(0)
	v_mul_f32_e64 v4, v28, v88
	v_mul_f32_e64 v5, v29, v89
	v_pk_mul_f32 v[6:7], v[26:27], v[86:87]
	v_pk_fma_f32 v[8:9], v[16:17], v[84:85], v[4:5]
	v_cvt_pk_bf16_f32 v3, v2, v3
	v_pk_fma_f32 v[14:15], v[14:15], v[82:83], v[6:7]
	v_pk_add_f32 v[26:27], v[8:9], v[30:31]
	v_cvt_pk_bf16_f32 v5, v4, v5
	v_cvt_pk_bf16_f32 v4, v6, v7
	ds_read_b128 v[6:9], v213 offset:10240
	v_pk_add_f32 v[28:29], v[14:15], v[32:33]
	ds_read_b128 v[14:17], v213 offset:11264
	v_cvt_pk_bf16_f32 v2, v94, v95
	s_waitcnt lgkmcnt(1)
	v_pk_mul_f32 v[30:31], v[6:7], v[82:83]
	v_mov_b64_e32 v[152:153], s[4:5]
	v_mfma_f32_32x32x16_bf16 v[34:49], v[10:13], v[2:5], v[34:49]
	v_mul_f32_e64 v2, v8, v84
	v_mul_f32_e64 v3, v9, v85
	s_waitcnt lgkmcnt(0)
	v_mul_f32_e64 v4, v16, v88
	v_mul_f32_e64 v5, v17, v89
	v_pk_mul_f32 v[14:15], v[14:15], v[86:87]
	v_pk_fma_f32 v[8:9], v[8:9], v[84:85], v[4:5]
	v_pk_fma_f32 v[6:7], v[6:7], v[82:83], v[14:15]
	v_cvt_pk_bf16_f32 v5, v4, v5
	v_cvt_pk_bf16_f32 v3, v2, v3
	v_cvt_pk_bf16_f32 v4, v14, v15
	v_pk_add_f32 v[32:33], v[8:9], v[90:91]
	v_pk_add_f32 v[90:91], v[6:7], v[92:93]
	ds_read_b128 v[6:9], v213 offset:34816
	ds_read_b128 v[14:17], v213 offset:4096
	v_cvt_pk_bf16_f32 v2, v30, v31
	s_mov_b32 s13, 0
	s_mov_b64 s[6:7], 0
	v_mfma_f32_32x32x16_bf16 v[50:65], v[10:13], v[2:5], v[50:65]
	ds_read_b128 v[2:5], v213 offset:5120
	ds_read_b128 v[10:13], v213 offset:12288
	s_waitcnt lgkmcnt(2)
	v_pk_mul_f32 v[30:31], v[16:17], v[76:77]
	v_pk_mul_f32 v[92:93], v[14:15], v[74:75]
	s_waitcnt lgkmcnt(1)
	v_pk_mul_f32 v[4:5], v[4:5], v[80:81]
	v_pk_mul_f32 v[94:95], v[2:3], v[78:79]
	v_pk_fma_f32 v[2:3], v[16:17], v[76:77], v[4:5]
	v_cvt_pk_bf16_f32 v5, v4, v5
	v_pk_add_f32 v[96:97], v[2:3], v[26:27]
	v_cvt_pk_bf16_f32 v3, v30, v31
	v_cvt_pk_bf16_f32 v4, v94, v95
	v_cvt_pk_bf16_f32 v2, v92, v93
	v_pk_fma_f32 v[14:15], v[14:15], v[74:75], v[94:95]
	s_waitcnt lgkmcnt(0)
	v_pk_mul_f32 v[30:31], v[10:11], v[74:75]
	v_mfma_f32_32x32x16_bf16 v[34:49], v[6:9], v[2:5], v[34:49]
	ds_read_b128 v[2:5], v213 offset:13312
	v_add_f32_e64 v98, v14, v28
	v_add_f32_e64 v99, v15, v29
	ds_read_b128 v[14:17], v213 offset:35840
	v_pk_mul_f32 v[26:27], v[12:13], v[76:77]
	s_waitcnt lgkmcnt(1)
	v_pk_mul_f32 v[4:5], v[4:5], v[80:81]
	v_pk_mul_f32 v[28:29], v[2:3], v[78:79]
	v_pk_fma_f32 v[2:3], v[12:13], v[76:77], v[4:5]
	v_pk_fma_f32 v[10:11], v[10:11], v[74:75], v[28:29]
	v_pk_add_f32 v[32:33], v[2:3], v[32:33]
	v_pk_add_f32 v[92:93], v[10:11], v[90:91]
	ds_read_b128 v[10:13], v213 offset:6144
	v_cvt_pk_bf16_f32 v5, v4, v5
	v_cvt_pk_bf16_f32 v3, v26, v27
	v_cvt_pk_bf16_f32 v4, v28, v29
	ds_read_b128 v[26:29], v213 offset:7168
	v_cvt_pk_bf16_f32 v2, v30, v31
	s_waitcnt lgkmcnt(1)
	v_pk_mul_f32 v[30:31], v[10:11], v[66:67]
	v_mfma_f32_32x32x16_bf16 v[50:65], v[6:9], v[2:5], v[50:65]
	v_mul_f32_e64 v2, v12, v68
	v_mul_f32_e64 v3, v13, v69
	s_waitcnt lgkmcnt(0)
	v_mul_f32_e64 v4, v28, v72
	v_mul_f32_e64 v5, v29, v73
	v_pk_mul_f32 v[6:7], v[26:27], v[70:71]
	v_pk_fma_f32 v[8:9], v[12:13], v[68:69], v[4:5]
	v_cvt_pk_bf16_f32 v3, v2, v3
	v_pk_fma_f32 v[10:11], v[10:11], v[66:67], v[6:7]
	v_pk_add_f32 v[94:95], v[8:9], v[96:97]
	v_cvt_pk_bf16_f32 v5, v4, v5
	v_cvt_pk_bf16_f32 v4, v6, v7
	ds_read_b128 v[6:9], v213 offset:14336
	v_pk_add_f32 v[96:97], v[10:11], v[98:99]
	ds_read_b128 v[10:13], v213 offset:15360
	v_cvt_pk_bf16_f32 v2, v30, v31
	s_waitcnt lgkmcnt(1)
	v_pk_mul_f32 v[30:31], v[6:7], v[66:67]
	v_mfma_f32_32x32x16_bf16 v[34:49], v[14:17], v[2:5], v[34:49]
	s_waitcnt lgkmcnt(0)
	v_mul_f32_e64 v10, v10, v70
	v_mul_f32_e64 v11, v11, v71
	v_mul_f32_e64 v2, v8, v68
	v_mul_f32_e64 v3, v9, v69
	v_pk_mul_f32 v[4:5], v[12:13], v[72:73]
	v_pk_fma_f32 v[6:7], v[6:7], v[66:67], v[10:11]
	v_pk_fma_f32 v[8:9], v[8:9], v[68:69], v[4:5]
	v_pk_add_f32 v[92:93], v[6:7], v[92:93]
	v_cvt_pk_bf16_f32 v3, v2, v3
	v_pk_add_f32 v[90:91], v[8:9], v[32:33]
	v_cvt_pk_bf16_f32 v5, v4, v5
	v_cvt_pk_bf16_f32 v4, v10, v11
	ds_read_b128 v[26:29], v213 offset:36864
	ds_read_b128 v[6:9], v213 offset:16384
	v_cvt_pk_bf16_f32 v2, v30, v31
	ds_read_b128 v[98:101], v213 offset:25600
	ds_read_b128 v[102:105], v213 offset:37888
	v_mfma_f32_32x32x16_bf16 v[50:65], v[14:17], v[2:5], v[50:65]
	ds_read_b128 v[2:5], v213 offset:17408
	ds_read_b128 v[30:33], v213 offset:24576
	s_waitcnt lgkmcnt(4)
	v_pk_mul_f32 v[12:13], v[6:7], v[18:19]
	v_pk_mul_f32 v[10:11], v[8:9], v[20:21]
	s_waitcnt lgkmcnt(1)
	v_pk_mul_f32 v[14:15], v[2:3], v[22:23]
	v_pk_mul_f32 v[22:23], v[98:99], v[22:23]
	v_pk_fma_f32 v[112:113], v[6:7], v[18:19], v[14:15]
	s_waitcnt lgkmcnt(0)
	v_pk_mul_f32 v[114:115], v[30:31], v[18:19]
	v_pk_fma_f32 v[118:119], v[30:31], v[18:19], v[22:23]
	v_pk_mul_f32 v[4:5], v[4:5], v[24:25]
	v_pk_mul_f32 v[106:107], v[32:33], v[20:21]
	v_pk_mul_f32 v[24:25], v[100:101], v[24:25]
	ds_read_b128 v[98:101], v213 offset:18432
	v_cvt_pk_bf16_f32 v19, v106, v107
	ds_read_b128 v[106:109], v213 offset:19456
	v_pk_fma_f32 v[110:111], v[8:9], v[20:21], v[4:5]
	v_cvt_pk_bf16_f32 v5, v4, v5
	v_cvt_pk_bf16_f32 v3, v10, v11
	v_cvt_pk_bf16_f32 v4, v14, v15
	s_waitcnt lgkmcnt(0)
	v_pk_mul_f32 v[106:107], v[106:107], v[86:87]
	v_cvt_pk_bf16_f32 v2, v12, v13
	v_pk_mul_f32 v[120:121], v[98:99], v[82:83]
	v_pk_mul_f32 v[108:109], v[108:109], v[88:89]
	v_pk_fma_f32 v[98:99], v[98:99], v[82:83], v[106:107]
	v_mfma_f32_32x32x16_bf16 v[2:17], v[26:29], v[2:5], 0
	v_cvt_pk_bf16_f32 v18, v114, v115
	v_mul_f32_e64 v114, v100, v84
	v_mul_f32_e64 v115, v101, v85
	v_fma_f32 v100, v100, v84, v108
	v_fma_f32 v101, v101, v85, v109
	v_pk_add_f32 v[124:125], v[98:99], v[112:113]
	v_pk_add_f32 v[122:123], v[100:101], v[110:111]
	v_cvt_pk_bf16_f32 v101, v108, v109
	v_cvt_pk_bf16_f32 v100, v106, v107
	ds_read_b128 v[106:109], v213 offset:26624
	v_pk_fma_f32 v[116:117], v[32:33], v[20:21], v[24:25]
	v_cvt_pk_bf16_f32 v21, v24, v25
	v_cvt_pk_bf16_f32 v20, v22, v23
	ds_read_b128 v[110:113], v213 offset:27648
	v_cvt_pk_bf16_f32 v99, v114, v115
	v_mfma_f32_32x32x16_bf16 v[18:33], v[26:29], v[18:21], 0
	v_cvt_pk_bf16_f32 v98, v120, v121
	s_waitcnt lgkmcnt(1)
	v_mul_f32_e64 v114, v106, v82
	v_mul_f32_e64 v115, v107, v83
	s_waitcnt lgkmcnt(0)
	v_pk_mul_f32 v[86:87], v[110:111], v[86:87]
	v_pk_mul_f32 v[88:89], v[112:113], v[88:89]
	v_pk_fma_f32 v[82:83], v[106:107], v[82:83], v[86:87]
	v_mfma_f32_32x32x16_bf16 v[2:17], v[102:105], v[98:101], v[2:17]
	v_mul_f32_e64 v98, v108, v84
	v_mul_f32_e64 v99, v109, v85
	v_fma_f32 v84, v108, v84, v88
	v_fma_f32 v85, v109, v85, v89
	v_add_f32_e64 v108, v82, v118
	v_add_f32_e64 v109, v83, v119
	v_cvt_pk_bf16_f32 v83, v98, v99
	v_pk_add_f32 v[106:107], v[84:85], v[116:117]
	v_cvt_pk_bf16_f32 v85, v88, v89
	v_cvt_pk_bf16_f32 v84, v86, v87
	ds_read_b128 v[86:89], v213 offset:38912
	ds_read_b128 v[98:101], v213 offset:20480
	v_cvt_pk_bf16_f32 v82, v114, v115
	s_waitcnt lgkmcnt(0)
	v_pk_mul_f32 v[110:111], v[100:101], v[76:77]
	v_mfma_f32_32x32x16_bf16 v[18:33], v[102:105], v[82:85], v[18:33]
	ds_read_b128 v[82:85], v213 offset:21504
	ds_read_b128 v[102:105], v213 offset:28672
	v_mul_f32_e64 v112, v98, v74
	v_mul_f32_e64 v113, v99, v75
	s_waitcnt lgkmcnt(1)
	v_pk_mul_f32 v[84:85], v[84:85], v[80:81]
	v_pk_mul_f32 v[114:115], v[82:83], v[78:79]
	v_pk_fma_f32 v[82:83], v[100:101], v[76:77], v[84:85]
	v_cvt_pk_bf16_f32 v85, v84, v85
	v_pk_add_f32 v[116:117], v[82:83], v[122:123]
	v_cvt_pk_bf16_f32 v83, v110, v111
	v_cvt_pk_bf16_f32 v84, v114, v115
	v_cvt_pk_bf16_f32 v82, v112, v113
	v_pk_fma_f32 v[98:99], v[98:99], v[74:75], v[114:115]
	s_waitcnt lgkmcnt(0)
	v_pk_mul_f32 v[112:113], v[102:103], v[74:75]
	v_mfma_f32_32x32x16_bf16 v[2:17], v[86:89], v[82:85], v[2:17]
	ds_read_b128 v[82:85], v213 offset:29696
	v_add_f32_e64 v118, v98, v124
	v_add_f32_e64 v119, v99, v125
	v_mul_f32_e64 v110, v104, v76
	v_mul_f32_e64 v111, v105, v77
	ds_read_b128 v[98:101], v213 offset:39936
	s_waitcnt lgkmcnt(1)
	v_pk_mul_f32 v[78:79], v[82:83], v[78:79]
	v_pk_mul_f32 v[80:81], v[84:85], v[80:81]
	v_pk_fma_f32 v[74:75], v[102:103], v[74:75], v[78:79]
	v_pk_fma_f32 v[76:77], v[104:105], v[76:77], v[80:81]
	v_pk_add_f32 v[104:105], v[74:75], v[108:109]
	v_pk_add_f32 v[102:103], v[76:77], v[106:107]
	v_cvt_pk_bf16_f32 v77, v80, v81
	v_cvt_pk_bf16_f32 v76, v78, v79
	ds_read_b128 v[78:81], v213 offset:22528
	ds_read_b128 v[82:85], v213 offset:23552
	v_cvt_pk_bf16_f32 v75, v110, v111
	v_cvt_pk_bf16_f32 v74, v112, v113
	s_waitcnt lgkmcnt(0)
	v_pk_mul_f32 v[82:83], v[82:83], v[70:71]
	v_mfma_f32_32x32x16_bf16 v[18:33], v[86:89], v[74:77], v[18:33]
	v_mul_f32_e64 v74, v80, v68
	v_mul_f32_e64 v75, v81, v69
	v_mul_f32_e64 v76, v84, v72
	v_mul_f32_e64 v77, v85, v73
	v_mul_f32_e64 v86, v78, v66
	v_mul_f32_e64 v87, v79, v67
	v_pk_fma_f32 v[80:81], v[80:81], v[68:69], v[76:77]
	v_pk_fma_f32 v[78:79], v[78:79], v[66:67], v[82:83]
	v_cvt_pk_bf16_f32 v75, v74, v75
	v_pk_add_f32 v[88:89], v[80:81], v[116:117]
	v_pk_add_f32 v[106:107], v[78:79], v[118:119]
	ds_read_b128 v[78:81], v213 offset:30720
	v_cvt_pk_bf16_f32 v77, v76, v77
	v_cvt_pk_bf16_f32 v76, v82, v83
	ds_read_b128 v[82:85], v213 offset:31744
	v_cvt_pk_bf16_f32 v74, v86, v87
	s_waitcnt lgkmcnt(0)
	v_pk_mul_f32 v[72:73], v[84:85], v[72:73]
	v_mfma_f32_32x32x16_bf16 v[2:17], v[98:101], v[74:77], v[2:17]
	v_mul_f32_e64 v74, v80, v68
	v_mul_f32_e64 v75, v81, v69
	v_fma_f32 v68, v80, v68, v72
	v_fma_f32 v69, v81, v69, v73
	v_mul_f32_e64 v70, v82, v70
	v_mul_f32_e64 v71, v83, v71
	v_pk_add_f32 v[84:85], v[68:69], v[102:103]
	v_cvt_pk_bf16_f32 v69, v72, v73
	v_pk_mov_b32 v[72:73], v[96:97], v[94:95] op_sel:[1,0]
	v_mov_b32_e32 v97, v95
	v_pk_add_f32 v[72:73], v[72:73], v[96:97]
	v_pk_mul_f32 v[76:77], v[78:79], v[66:67]
	v_pk_fma_f32 v[66:67], v[78:79], v[66:67], v[70:71]
	v_pk_add_f32 v[72:73], v[72:73], v[72:73] op_sel:[0,1] op_sel_hi:[1,0]
	v_pk_add_f32 v[86:87], v[66:67], v[104:105]
	v_mov_b32_e32 v66, v72
	s_nop 1
	v_permlane32_swap_b32_e32 v72, v66
	v_add_f32_e32 v66, v72, v66
	v_cvt_pk_bf16_f32 v67, v74, v75
	v_rcp_f32_e32 v74, v66
	v_cvt_pk_bf16_f32 v68, v70, v71
	v_cvt_pk_bf16_f32 v66, v76, v77
	v_pk_mul_f32 v[70:71], v[46:47], v[74:75] op_sel_hi:[1,0]
	s_nop 0
	v_mfma_f32_32x32x16_bf16 v[18:33], v[98:101], v[66:69], v[18:33]
	v_mul_f32_e64 v66, v42, v74
	v_mul_f32_e64 v67, v43, v74
	v_pk_mov_b32 v[42:43], v[92:93], v[90:91] op_sel:[1,0]
	v_mov_b32_e32 v93, v91
	v_pk_add_f32 v[42:43], v[42:43], v[92:93]
	v_pk_mul_f32 v[68:69], v[44:45], v[74:75] op_sel_hi:[1,0]
	v_pk_add_f32 v[42:43], v[42:43], v[42:43] op_sel:[0,1] op_sel_hi:[1,0]
	v_pk_mov_b32 v[44:45], v[106:107], v[88:89] op_sel:[1,0]
	v_mov_b32_e32 v43, v42
	s_nop 1
	v_permlane32_swap_b32_e32 v42, v43
	v_add_f32_e32 v42, v42, v43
	v_rcp_f32_e32 v42, v42
	v_mov_b32_e32 v107, v89
	v_pk_add_f32 v[44:45], v[44:45], v[106:107]
	v_pk_mul_f32 v[72:73], v[48:49], v[74:75] op_sel_hi:[1,0]
	v_pk_add_f32 v[44:45], v[44:45], v[44:45] op_sel:[0,1] op_sel_hi:[1,0]
	v_pk_mul_f32 v[36:37], v[36:37], v[74:75] op_sel_hi:[1,0]
	v_pk_mul_f32 v[38:39], v[38:39], v[74:75] op_sel_hi:[1,0]
	v_pk_mul_f32 v[40:41], v[40:41], v[74:75] op_sel_hi:[1,0]
	v_pk_mul_f32 v[34:35], v[34:35], v[74:75] op_sel_hi:[1,0]
	v_pk_mul_f32 v[74:75], v[58:59], v[42:43] op_sel_hi:[1,0]
	v_pk_mul_f32 v[78:79], v[60:61], v[42:43] op_sel_hi:[1,0]
	v_pk_mul_f32 v[80:81], v[62:63], v[42:43] op_sel_hi:[1,0]
	v_pk_mul_f32 v[82:83], v[64:65], v[42:43] op_sel_hi:[1,0]
	v_pk_mul_f32 v[92:93], v[52:53], v[42:43] op_sel_hi:[1,0]
	v_mov_b32_e32 v43, v44
	s_nop 1
	v_permlane32_swap_b32_e32 v44, v43
	v_add_f32_e32 v43, v44, v43
	v_rcp_f32_e32 v76, v43
	v_pk_mul_f32 v[96:97], v[54:55], v[42:43] op_sel_hi:[1,0]
	v_pk_mul_f32 v[94:95], v[56:57], v[42:43] op_sel_hi:[1,0]
	v_pk_mul_f32 v[98:99], v[50:51], v[42:43] op_sel_hi:[1,0]
	v_pk_mul_f32 v[100:101], v[4:5], v[76:77] op_sel_hi:[1,0]
	v_pk_mov_b32 v[4:5], v[86:87], v[84:85] op_sel:[1,0]
	v_mov_b32_e32 v87, v85
	v_pk_add_f32 v[4:5], v[4:5], v[86:87]
	v_pk_mul_f32 v[102:103], v[6:7], v[76:77] op_sel_hi:[1,0]
	v_pk_add_f32 v[104:105], v[4:5], v[4:5] op_sel:[0,1] op_sel_hi:[1,0]
	v_cvt_pk_bf16_f32 v7, v40, v41
	ds_read_b128 v[84:87], v150 offset:52224
	ds_read_b128 v[50:53], v150 offset:35840
	ds_read_b128 v[54:57], v150 offset:36864
	ds_read_b128 v[58:61], v150 offset:37888
	ds_read_b128 v[62:65], v150 offset:38912
	v_cvt_pk_bf16_f32 v6, v38, v39
	v_cvt_pk_bf16_f32 v5, v36, v37
	v_cvt_pk_bf16_f32 v4, v34, v35
	ds_read_b128 v[88:91], v150 offset:53248
	ds_read_b128 v[34:37], v150 offset:39936
	ds_read_b128 v[38:41], v150 offset:40960
	ds_read_b128 v[42:45], v150 offset:41984
	ds_read_b128 v[46:49], v150 offset:43008
	v_cvt_pk_bf16_f32 v95, v94, v95
	v_cvt_pk_bf16_f32 v94, v96, v97
	v_cvt_pk_bf16_f32 v93, v92, v93
	v_cvt_pk_bf16_f32 v92, v98, v99
	s_waitcnt lgkmcnt(5)
	v_mfma_f32_32x32x16_bf16 v[50:65], v[84:87], v[4:7], v[50:65]
	v_mul_f32_e64 v10, v10, v76
	v_mul_f32_e64 v11, v11, v76
	v_mul_f32_e64 v12, v12, v76
	v_mul_f32_e64 v13, v13, v76
	v_mul_f32_e64 v8, v8, v76
	v_mul_f32_e64 v9, v9, v76
	v_mov_b32_e32 v77, v104
	s_nop 1
	v_permlane32_swap_b32_e32 v104, v77
	v_cvt_pk_bf16_f32 v73, v72, v73
	s_waitcnt lgkmcnt(0)
	v_mfma_f32_32x32x16_bf16 v[34:49], v[84:87], v[92:95], v[34:49]
	v_cvt_pk_bf16_f32 v72, v70, v71
	v_cvt_pk_bf16_f32 v70, v66, v67
	v_add_f32_e32 v66, v104, v77
	v_cvt_pk_bf16_f32 v71, v68, v69
	v_rcp_f32_e32 v104, v66
	v_cvt_pk_bf16_f32 v69, v82, v83
	v_cvt_pk_bf16_f32 v68, v80, v81
	v_cvt_pk_bf16_f32 v67, v78, v79
	v_cvt_pk_bf16_f32 v66, v74, v75
	ds_read_b128 v[78:81], v150 offset:54272
	v_mfma_f32_32x32x16_bf16 v[50:65], v[88:91], v[70:73], v[50:65]
	v_mul_f32_e64 v2, v2, v76
	v_mul_f32_e64 v3, v3, v76
	v_mul_f32_e64 v20, v20, v104
	v_mul_f32_e64 v21, v21, v104
	v_cvt_pk_bf16_f32 v85, v8, v9
	v_cvt_pk_bf16_f32 v82, v2, v3
	v_pk_mul_f32 v[2:3], v[22:23], v[104:105] op_sel_hi:[1,0]
	v_pk_mul_f32 v[8:9], v[24:25], v[104:105] op_sel_hi:[1,0]
	v_pk_mul_f32 v[18:19], v[18:19], v[104:105] op_sel_hi:[1,0]
	v_mfma_f32_32x32x16_bf16 v[34:49], v[88:91], v[66:69], v[34:49]
	v_cvt_pk_bf16_f32 v84, v102, v103
	v_cvt_pk_bf16_f32 v83, v100, v101
	ds_read_b128 v[86:89], v150 offset:55296
	v_cvt_pk_bf16_f32 v99, v8, v9
	v_cvt_pk_bf16_f32 v98, v2, v3
	v_cvt_pk_bf16_f32 v97, v20, v21
	v_cvt_pk_bf16_f32 v96, v18, v19
	s_waitcnt lgkmcnt(1)
	v_mfma_f32_32x32x16_bf16 v[50:65], v[78:81], v[82:85], v[50:65]
	v_mul_f32_e64 v2, v14, v76
	v_mul_f32_e64 v3, v15, v76
	v_mul_f32_e64 v8, v16, v76
	v_mul_f32_e64 v9, v17, v76
	v_mul_f32_e64 v14, v26, v104
	v_mul_f32_e64 v15, v27, v104
	v_cvt_pk_bf16_f32 v77, v8, v9
	v_cvt_pk_bf16_f32 v76, v2, v3
	v_cvt_pk_bf16_f32 v74, v10, v11
	v_pk_mul_f32 v[2:3], v[28:29], v[104:105] op_sel_hi:[1,0]
	v_mfma_f32_32x32x16_bf16 v[34:49], v[78:81], v[96:99], v[34:49]
	v_mul_f32_e64 v8, v30, v104
	v_mul_f32_e64 v9, v31, v104
	v_mul_f32_e64 v10, v32, v104
	v_mul_f32_e64 v11, v33, v104
	v_cvt_pk_bf16_f32 v75, v12, v13
	v_cvt_pk_bf16_f32 v81, v10, v11
	v_cvt_pk_bf16_f32 v80, v8, v9
	v_cvt_pk_bf16_f32 v79, v2, v3
	v_cvt_pk_bf16_f32 v78, v14, v15
	s_waitcnt lgkmcnt(0)
	v_mfma_f32_32x32x16_bf16 v[50:65], v[86:89], v[74:77], v[50:65]
	v_mfma_f32_32x32x16_bf16 v[34:49], v[86:89], v[78:81], v[34:49]
	ds_read_b128 v[86:89], v150 offset:56320
	ds_read_b128 v[18:21], v150 offset:44032
	ds_read_b128 v[22:25], v150 offset:45056
	ds_read_b128 v[26:29], v150 offset:46080
	ds_read_b128 v[30:33], v150 offset:47104
	ds_read_b128 v[100:103], v150 offset:57344
	s_waitcnt lgkmcnt(1)
	v_mfma_f32_32x32x16_bf16 v[18:33], v[86:89], v[4:7], v[18:33]
	ds_read_b128 v[2:5], v150 offset:48128
	ds_read_b128 v[6:9], v150 offset:49152
	ds_read_b128 v[10:13], v150 offset:50176
	ds_read_b128 v[14:17], v150 offset:51200
	s_waitcnt lgkmcnt(0)
	v_mfma_f32_32x32x16_bf16 v[2:17], v[86:89], v[92:95], v[2:17]
	v_mfma_f32_32x32x16_bf16 v[18:33], v[100:103], v[70:73], v[18:33]
	v_mfma_f32_32x32x16_bf16 v[2:17], v[100:103], v[66:69], v[2:17]
	ds_read_b128 v[66:69], v150 offset:58368
	ds_read_b128 v[70:73], v150 offset:59392
	s_waitcnt lgkmcnt(1)
	v_mfma_f32_32x32x16_bf16 v[18:33], v[66:69], v[82:85], v[18:33]
	v_mfma_f32_32x32x16_bf16 v[2:17], v[66:69], v[96:99], v[2:17]
	s_waitcnt lgkmcnt(0)
	v_mfma_f32_32x32x16_bf16 v[18:33], v[70:73], v[74:77], v[18:33]
	v_mfma_f32_32x32x16_bf16 v[2:17], v[70:73], v[78:81], v[2:17]
	s_nop 10
	v_mul_f32_e64 v66, v22, v22
	v_mul_f32_e64 v67, v23, v23
	v_mul_f32_e64 v68, v30, v30
	v_mul_f32_e64 v69, v31, v31
	v_mul_f32_e64 v70, v24, v24
	v_mul_f32_e64 v71, v25, v25
	v_pk_mul_f32 v[72:73], v[32:33], v[32:33]
	v_pk_mul_f32 v[74:75], v[20:21], v[20:21]
	v_pk_mul_f32 v[76:77], v[28:29], v[28:29]
	v_pk_mul_f32 v[78:79], v[26:27], v[26:27]
	v_pk_mul_f32 v[80:81], v[18:19], v[18:19]
	v_pk_fma_f32 v[78:79], v[58:59], v[58:59], v[78:79]
	v_pk_fma_f32 v[76:77], v[60:61], v[60:61], v[76:77]
	v_pk_fma_f32 v[74:75], v[52:53], v[52:53], v[74:75]
	v_pk_fma_f32 v[72:73], v[64:65], v[64:65], v[72:73]
	v_pk_fma_f32 v[70:71], v[56:57], v[56:57], v[70:71]
	v_pk_fma_f32 v[68:69], v[62:63], v[62:63], v[68:69]
	v_pk_fma_f32 v[66:67], v[54:55], v[54:55], v[66:67]
	v_pk_fma_f32 v[80:81], v[50:51], v[50:51], v[80:81]
	v_pk_add_f32 v[66:67], v[66:67], v[68:69]
	v_pk_add_f32 v[68:69], v[70:71], v[72:73]
	v_pk_add_f32 v[70:71], v[74:75], v[76:77]
	v_pk_add_f32 v[72:73], v[80:81], v[78:79]
	v_pk_add_f32 v[68:69], v[70:71], v[68:69]
	v_pk_add_f32 v[66:67], v[72:73], v[66:67]
	v_pk_mul_f32 v[72:73], v[14:15], v[14:15]
	v_pk_mov_b32 v[70:71], v[66:67], v[68:69] op_sel:[1,0]
	v_mov_b32_e32 v67, v69
	v_pk_add_f32 v[66:67], v[70:71], v[66:67]
	v_pk_mul_f32 v[70:71], v[6:7], v[6:7]
	v_pk_mul_f32 v[74:75], v[8:9], v[8:9]
	v_pk_mul_f32 v[76:77], v[16:17], v[16:17]
	v_pk_mul_f32 v[78:79], v[4:5], v[4:5]
	v_pk_mul_f32 v[80:81], v[12:13], v[12:13]
	v_pk_mul_f32 v[82:83], v[10:11], v[10:11]
	v_pk_mul_f32 v[84:85], v[2:3], v[2:3]
	v_pk_fma_f32 v[82:83], v[42:43], v[42:43], v[82:83]
	v_pk_fma_f32 v[80:81], v[44:45], v[44:45], v[80:81]
	v_pk_fma_f32 v[78:79], v[36:37], v[36:37], v[78:79]
	v_pk_fma_f32 v[76:77], v[48:49], v[48:49], v[76:77]
	v_pk_fma_f32 v[74:75], v[40:41], v[40:41], v[74:75]
	v_pk_fma_f32 v[72:73], v[46:47], v[46:47], v[72:73]
	v_pk_fma_f32 v[70:71], v[38:39], v[38:39], v[70:71]
	v_pk_fma_f32 v[84:85], v[34:35], v[34:35], v[84:85]
	v_pk_add_f32 v[70:71], v[70:71], v[72:73]
	v_pk_add_f32 v[72:73], v[74:75], v[76:77]
	v_pk_add_f32 v[74:75], v[78:79], v[80:81]
	v_pk_add_f32 v[76:77], v[84:85], v[82:83]
	v_pk_add_f32 v[72:73], v[74:75], v[72:73]
	v_pk_add_f32 v[70:71], v[76:77], v[70:71]
	v_pk_add_f32 v[66:67], v[66:67], v[66:67] op_sel:[0,1] op_sel_hi:[1,0]
	v_pk_mov_b32 v[74:75], v[70:71], v[72:73] op_sel:[1,0]
	v_mov_b32_e32 v71, v73
	v_pk_add_f32 v[70:71], v[74:75], v[70:71]
	v_mov_b32_e32 v69, v66
	v_pk_add_f32 v[70:71], v[70:71], v[70:71] op_sel:[0,1] op_sel_hi:[1,0]
	s_nop 0
	v_permlane32_swap_b32_e32 v66, v69
	v_mov_b32_e32 v68, v70
	s_nop 1
	v_permlane32_swap_b32_e32 v70, v68
	v_mov_b32_e32 v71, v66
	v_pk_add_f32 v[66:67], v[70:71], v[68:69]
	s_nop 0
	v_pk_fma_f32 v[66:67], v[66:67], s[0:1], v[152:153] op_sel_hi:[1,0,0]
	s_mov_b32 s1, 0x800000
	v_mul_f32_e32 v68, 0x4b800000, v67
	v_cmp_gt_f32_e32 vcc, s1, v67
	s_nop 1
	v_cndmask_b32_e32 v67, v67, v68, vcc
	v_rsq_f32_e32 v67, v67
	s_nop 0
	v_mul_f32_e32 v68, 0x45800000, v67
	v_cndmask_b32_e32 v68, v67, v68, vcc
	v_pk_mul_f32 v[158:159], v[50:51], v[68:69] op_sel_hi:[1,0]
	v_pk_mul_f32 v[50:51], v[18:19], v[68:69] op_sel_hi:[1,0]
	v_mul_f32_e32 v18, 0x4b800000, v66
	v_cmp_gt_f32_e32 vcc, s1, v66
	v_pk_mul_f32 v[80:81], v[60:61], v[68:69] op_sel_hi:[1,0]
	v_pk_mul_f32 v[60:61], v[28:29], v[68:69] op_sel_hi:[1,0]
	v_cndmask_b32_e32 v18, v66, v18, vcc
	v_rsq_f32_e32 v18, v18
	v_pk_mul_f32 v[78:79], v[58:59], v[68:69] op_sel_hi:[1,0]
	v_pk_mul_f32 v[160:161], v[52:53], v[68:69] op_sel_hi:[1,0]
	v_pk_mul_f32 v[82:83], v[54:55], v[68:69] op_sel_hi:[1,0]
	v_mul_f32_e32 v19, 0x45800000, v18
	v_cndmask_b32_e32 v28, v18, v19, vcc
	v_pk_mul_f32 v[168:169], v[56:57], v[68:69] op_sel_hi:[1,0]
	v_pk_mul_f32 v[58:59], v[26:27], v[68:69] op_sel_hi:[1,0]
	v_pk_mul_f32 v[52:53], v[20:21], v[68:69] op_sel_hi:[1,0]
	v_pk_mul_f32 v[54:55], v[22:23], v[68:69] op_sel_hi:[1,0]
	v_pk_mul_f32 v[56:57], v[24:25], v[68:69] op_sel_hi:[1,0]
	v_pk_mul_f32 v[18:19], v[42:43], v[28:29] op_sel_hi:[1,0]
	v_pk_mul_f32 v[20:21], v[44:45], v[28:29] op_sel_hi:[1,0]
	v_pk_mul_f32 v[22:23], v[46:47], v[28:29] op_sel_hi:[1,0]
	v_pk_mul_f32 v[26:27], v[48:49], v[28:29] op_sel_hi:[1,0]
	v_pk_mul_f32 v[162:163], v[34:35], v[28:29] op_sel_hi:[1,0]
	v_pk_mul_f32 v[164:165], v[36:37], v[28:29] op_sel_hi:[1,0]
	v_pk_mul_f32 v[166:167], v[38:39], v[28:29] op_sel_hi:[1,0]
	v_pk_mul_f32 v[24:25], v[40:41], v[28:29] op_sel_hi:[1,0]
	v_pk_mul_f32 v[104:105], v[2:3], v[28:29] op_sel_hi:[1,0]
	v_pk_mul_f32 v[112:113], v[4:5], v[28:29] op_sel_hi:[1,0]
	ds_read_b128 v[2:5], v150 offset:60416
	ds_read_b128 v[34:37], v174 offset:32768
	ds_read_b128 v[38:41], v174 offset:32800
	ds_read_b128 v[42:45], v174 offset:32832
	ds_read_b128 v[46:49], v174 offset:32864
	v_cvt_pk_bf16_f32 v129, v168, v169
	v_cvt_pk_bf16_f32 v128, v82, v83
	v_cvt_pk_bf16_f32 v127, v160, v161
	v_cvt_pk_bf16_f32 v126, v158, v159
	v_cvt_pk_bf16_f32 v137, v24, v25
	v_cvt_pk_bf16_f32 v136, v166, v167
	v_cvt_pk_bf16_f32 v135, v164, v165
	s_waitcnt lgkmcnt(0)
	v_mfma_f32_32x32x16_bf16 v[86:101], v[2:5], v[126:129], v[34:49]
	v_cvt_pk_bf16_f32 v134, v162, v163
	v_mul_f32_e64 v84, v62, v68
	v_mul_f32_e64 v85, v63, v68
	v_mul_f32_e64 v170, v64, v68
	v_mul_f32_e64 v171, v65, v68
	v_pk_mul_f32 v[62:63], v[30:31], v[68:69] op_sel_hi:[1,0]
	v_pk_mul_f32 v[64:65], v[32:33], v[68:69] op_sel_hi:[1,0]
	v_pk_mul_f32 v[116:117], v[6:7], v[28:29] op_sel_hi:[1,0]
	v_pk_mul_f32 v[154:155], v[8:9], v[28:29] op_sel_hi:[1,0]
	v_mfma_f32_32x32x16_bf16 v[34:49], v[2:5], v[134:137], v[34:49]
	ds_read_b128 v[6:9], v150 offset:61440
	ds_read_b128 v[66:69], v174 offset:32896
	ds_read_b128 v[106:109], v150 offset:64512
	v_cvt_pk_bf16_f32 v125, v170, v171
	v_cvt_pk_bf16_f32 v124, v84, v85
	v_cvt_pk_bf16_f32 v123, v80, v81
	v_cvt_pk_bf16_f32 v122, v78, v79
	v_cvt_pk_bf16_f32 v149, v26, v27
	v_cvt_pk_bf16_f32 v148, v22, v23
	v_cvt_pk_bf16_f32 v147, v20, v21
	v_cvt_pk_bf16_f32 v146, v18, v19
	s_waitcnt lgkmcnt(2)
	v_mfma_f32_32x32x16_bf16 v[86:101], v[6:9], v[122:125], v[86:101]
	v_mul_f32_e64 v102, v10, v28
	v_mul_f32_e64 v103, v11, v28
	v_mul_f32_e64 v110, v12, v28
	v_mul_f32_e64 v111, v13, v28
	v_mul_f32_e64 v114, v14, v28
	v_mul_f32_e64 v115, v15, v28
	v_pk_mul_f32 v[156:157], v[16:17], v[28:29] op_sel_hi:[1,0]
	ds_read_b128 v[176:179], v174 offset:33536
	ds_read_b128 v[180:183], v174 offset:33568
	ds_read_b128 v[184:187], v174 offset:33600
	ds_read_b128 v[28:31], v174 offset:33632
	ds_read_b128 v[188:191], v174 offset:33792
	ds_read_b128 v[192:195], v174 offset:33824
	ds_read_b128 v[196:199], v174 offset:33856
	ds_read_b128 v[200:203], v174 offset:33888
	ds_read_b128 v[204:207], v150 offset:62464
	v_cvt_pk_bf16_f32 v133, v56, v57
	v_mfma_f32_32x32x16_bf16 v[34:49], v[6:9], v[146:149], v[34:49]
	v_cvt_pk_bf16_f32 v132, v54, v55
	v_cvt_pk_bf16_f32 v131, v52, v53
	v_cvt_pk_bf16_f32 v130, v50, v51
	ds_read_b128 v[70:73], v174 offset:33664
	ds_read_b128 v[74:77], v174 offset:33920
	ds_read_b128 v[208:211], v150 offset:63488
	v_cvt_pk_bf16_f32 v145, v154, v155
	v_cvt_pk_bf16_f32 v144, v116, v117
	v_cvt_pk_bf16_f32 v143, v112, v113
	v_cvt_pk_bf16_f32 v142, v104, v105
	s_waitcnt lgkmcnt(3)
	v_mfma_f32_32x32x16_bf16 v[86:101], v[204:207], v[130:133], v[86:101]
	v_cvt_pk_bf16_f32 v121, v64, v65
	v_cvt_pk_bf16_f32 v120, v62, v63
	v_cvt_pk_bf16_f32 v119, v60, v61
	v_cvt_pk_bf16_f32 v118, v58, v59
	v_cvt_pk_bf16_f32 v141, v156, v157
	v_cvt_pk_bf16_f32 v140, v114, v115
	v_cvt_pk_bf16_f32 v139, v110, v111
	v_mfma_f32_32x32x16_bf16 v[34:49], v[204:207], v[142:145], v[34:49]
	v_cvt_pk_bf16_f32 v138, v102, v103
	v_fma_f32 v16, v30, v170, v202
	v_fma_f32 v17, v31, v171, v203
	v_fma_f32 v14, v28, v84, v200
	v_fma_f32 v15, v29, v85, v201
	v_pk_fma_f32 v[12:13], v[186:187], v[80:81], v[198:199]
	v_pk_fma_f32 v[10:11], v[184:185], v[78:79], v[196:197]
	v_pk_fma_f32 v[8:9], v[182:183], v[168:169], v[194:195]
	s_waitcnt lgkmcnt(0)
	v_mfma_f32_32x32x16_bf16 v[86:101], v[208:211], v[118:121], v[86:101]
	v_fma_f32 v6, v180, v82, v192
	v_fma_f32 v7, v181, v83, v193
	ds_read_b128 v[78:81], v174 offset:33760
	ds_read_b128 v[82:85], v174 offset:33248
	v_fma_f32 v4, v178, v160, v190
	v_fma_f32 v5, v179, v161, v191
	v_pk_fma_f32 v[2:3], v[176:177], v[158:159], v[188:189]
	v_pk_fma_f32 v[32:33], v[30:31], v[26:27], v[202:203]
	v_pk_fma_f32 v[30:31], v[28:29], v[22:23], v[200:201]
	v_pk_fma_f32 v[28:29], v[186:187], v[20:21], v[198:199]
	v_pk_fma_f32 v[26:27], v[184:185], v[18:19], v[196:197]
	v_pk_fma_f32 v[24:25], v[182:183], v[24:25], v[194:195]
	v_pk_fma_f32 v[22:23], v[180:181], v[166:167], v[192:193]
	v_pk_fma_f32 v[20:21], v[178:179], v[164:165], v[190:191]
	v_pk_fma_f32 v[18:19], v[176:177], v[162:163], v[188:189]
	ds_read_b128 v[158:161], v174 offset:33696
	ds_read_b128 v[162:165], v174 offset:33728
	ds_read_b128 v[166:169], v174 offset:33952
	ds_read_b128 v[176:179], v174 offset:33984
	ds_read_b128 v[180:183], v174 offset:34016
	ds_read_b128 v[184:187], v212 offset:11264
	v_mfma_f32_32x32x16_bf16 v[34:49], v[208:211], v[138:141], v[34:49]
	v_cvt_pk_bf16_f32 v86, v86, v87
	v_cvt_pk_bf16_f32 v87, v88, v89
	v_cvt_pk_bf16_f32 v88, v90, v91
	v_cvt_pk_bf16_f32 v89, v92, v93
	ds_read_b128 v[90:93], v212 offset:12288
	v_pk_max_i16 v86, v86, 0
	v_pk_max_i16 v87, v87, 0
	v_pk_max_i16 v88, v88, 0
	v_pk_max_i16 v89, v89, 0
	s_nop 1
	s_nop 5
	v_cvt_pk_bf16_f32 v188, v34, v35
	v_cvt_pk_bf16_f32 v189, v36, v37
	v_cvt_pk_bf16_f32 v190, v38, v39
	v_cvt_pk_bf16_f32 v191, v40, v41
	s_waitcnt lgkmcnt(1)
	v_mfma_f32_32x32x16_bf16 v[2:17], v[184:187], v[86:89], v[2:17]
	v_pk_max_i16 v188, v188, 0
	v_pk_max_i16 v189, v189, 0
	v_pk_max_i16 v190, v190, 0
	v_pk_max_i16 v191, v191, 0
	s_nop 1
	v_cvt_pk_bf16_f32 v94, v94, v95
	v_cvt_pk_bf16_f32 v95, v96, v97
	v_cvt_pk_bf16_f32 v96, v98, v99
	v_cvt_pk_bf16_f32 v97, v100, v101
	v_cvt_pk_bf16_f32 v98, v42, v43
	v_cvt_pk_bf16_f32 v99, v44, v45
	v_mfma_f32_32x32x16_bf16 v[18:33], v[184:187], v[188:191], v[18:33]
	ds_read_b128 v[184:187], v212 offset:19456
	v_cvt_pk_bf16_f32 v100, v46, v47
	v_cvt_pk_bf16_f32 v101, v48, v49
	v_fma_f32 v64, v80, v64, v182
	v_fma_f32 v65, v81, v65, v183
	v_pk_fma_f32 v[62:63], v[78:79], v[62:63], v[180:181]
	v_pk_fma_f32 v[60:61], v[164:165], v[60:61], v[178:179]
	v_pk_fma_f32 v[58:59], v[162:163], v[58:59], v[176:177]
	v_pk_max_i16 v94, v94, 0
	v_pk_max_i16 v95, v95, 0
	v_pk_max_i16 v96, v96, 0
	v_pk_max_i16 v97, v97, 0
	s_nop 1
	v_pk_max_i16 v98, v98, 0
	v_pk_max_i16 v99, v99, 0
	v_pk_max_i16 v100, v100, 0
	v_pk_max_i16 v101, v101, 0
	s_nop 1
	v_pk_fma_f32 v[56:57], v[160:161], v[56:57], v[168:169]
	s_waitcnt lgkmcnt(1)
	v_mfma_f32_32x32x16_bf16 v[2:17], v[90:93], v[94:97], v[2:17]
	v_fma_f32 v54, v158, v54, v166
	v_fma_f32 v55, v159, v55, v167
	v_fma_f32 v52, v72, v52, v76
	v_fma_f32 v53, v73, v53, v77
	v_fma_f32 v50, v70, v50, v74
	v_fma_f32 v51, v71, v51, v75
	v_pk_fma_f32 v[48:49], v[80:81], v[156:157], v[182:183]
	v_pk_fma_f32 v[46:47], v[78:79], v[114:115], v[180:181]
	v_pk_fma_f32 v[44:45], v[164:165], v[110:111], v[178:179]
	v_pk_fma_f32 v[42:43], v[162:163], v[102:103], v[176:177]
	v_mfma_f32_32x32x16_bf16 v[18:33], v[90:93], v[98:101], v[18:33]
	ds_read_b128 v[90:93], v212 offset:20480
	v_fma_f32 v40, v160, v154, v168
	v_fma_f32 v41, v161, v155, v169
	v_fma_f32 v38, v158, v116, v166
	v_fma_f32 v39, v159, v117, v167
	v_pk_fma_f32 v[36:37], v[72:73], v[112:113], v[76:77]
	v_pk_fma_f32 v[34:35], v[70:71], v[104:105], v[74:75]
	s_waitcnt lgkmcnt(1)
	v_mfma_f32_32x32x16_bf16 v[50:65], v[184:187], v[86:89], v[50:65]
	ds_read_b128 v[70:73], v174 offset:32928
	ds_read_b128 v[74:77], v174 offset:32960
	ds_read_b128 v[78:81], v174 offset:32992
	ds_read_b128 v[86:89], v174 offset:33024
	ds_read_b128 v[110:113], v212 offset:1024
	v_mfma_f32_32x32x16_bf16 v[34:49], v[184:187], v[188:191], v[34:49]
	s_waitcnt lgkmcnt(5)
	v_mfma_f32_32x32x16_bf16 v[50:65], v[90:93], v[94:97], v[50:65]
	v_mfma_f32_32x32x16_bf16 v[34:49], v[90:93], v[98:101], v[34:49]
	s_waitcnt lgkmcnt(2)
	v_mfma_f32_32x32x16_bf16 v[90:105], v[106:109], v[126:129], v[66:81]
	v_mfma_f32_32x32x16_bf16 v[66:81], v[106:109], v[134:137], v[66:81]
	ds_read_b128 v[106:109], v212 offset:0
	s_waitcnt lgkmcnt(0)
	v_mfma_f32_32x32x16_bf16 v[90:105], v[106:109], v[122:125], v[90:105]
	v_mfma_f32_32x32x16_bf16 v[66:81], v[106:109], v[146:149], v[66:81]
	ds_read_b128 v[106:109], v212 offset:2048
	v_mfma_f32_32x32x16_bf16 v[90:105], v[110:113], v[130:133], v[90:105]
	v_mfma_f32_32x32x16_bf16 v[66:81], v[110:113], v[142:145], v[66:81]
	ds_read_b128 v[110:113], v212 offset:13312
	s_waitcnt lgkmcnt(1)
	v_mfma_f32_32x32x16_bf16 v[90:105], v[106:109], v[118:121], v[90:105]
	v_mfma_f32_32x32x16_bf16 v[66:81], v[106:109], v[138:141], v[66:81]
	s_nop 10
	v_cvt_pk_bf16_f32 v90, v90, v91
	v_cvt_pk_bf16_f32 v91, v92, v93
	v_cvt_pk_bf16_f32 v92, v94, v95
	v_cvt_pk_bf16_f32 v94, v98, v99
	v_cvt_pk_bf16_f32 v95, v100, v101
	ds_read_b128 v[98:101], v212 offset:21504
	v_cvt_pk_bf16_f32 v66, v66, v67
	v_cvt_pk_bf16_f32 v67, v68, v69
	v_cvt_pk_bf16_f32 v68, v70, v71
	v_cvt_pk_bf16_f32 v93, v96, v97
	v_cvt_pk_bf16_f32 v69, v72, v73
	ds_read_b128 v[70:73], v212 offset:14336
	v_pk_max_i16 v90, v90, 0
	v_pk_max_i16 v91, v91, 0
	v_pk_max_i16 v92, v92, 0
	v_pk_max_i16 v93, v93, 0
	s_nop 1
	v_pk_max_i16 v66, v66, 0
	v_pk_max_i16 v67, v67, 0
	v_pk_max_i16 v68, v68, 0
	v_pk_max_i16 v69, v69, 0
	s_nop 1
	v_cvt_pk_bf16_f32 v96, v102, v103
	s_waitcnt lgkmcnt(2)
	v_mfma_f32_32x32x16_bf16 v[2:17], v[110:113], v[90:93], v[2:17]
	v_cvt_pk_bf16_f32 v97, v104, v105
	v_cvt_pk_bf16_f32 v74, v74, v75
	v_cvt_pk_bf16_f32 v75, v76, v77
	v_cvt_pk_bf16_f32 v76, v78, v79
	v_cvt_pk_bf16_f32 v77, v80, v81
	v_pk_max_i16 v94, v94, 0
	v_pk_max_i16 v95, v95, 0
	v_pk_max_i16 v96, v96, 0
	v_pk_max_i16 v97, v97, 0
	s_nop 1
	v_pk_max_i16 v74, v74, 0
	v_pk_max_i16 v75, v75, 0
	v_pk_max_i16 v76, v76, 0
	v_pk_max_i16 v77, v77, 0
	s_nop 1
	v_mfma_f32_32x32x16_bf16 v[18:33], v[110:113], v[66:69], v[18:33]
	s_waitcnt lgkmcnt(1)
	v_mfma_f32_32x32x16_bf16 v[34:49], v[98:101], v[66:69], v[34:49]
	ds_read_b128 v[66:69], v212 offset:22528
	v_mfma_f32_32x32x16_bf16 v[50:65], v[98:101], v[90:93], v[50:65]
	s_waitcnt lgkmcnt(1)
	v_mfma_f32_32x32x16_bf16 v[2:17], v[70:73], v[94:97], v[2:17]
	v_mfma_f32_32x32x16_bf16 v[18:33], v[70:73], v[74:77], v[18:33]
	ds_read_b128 v[78:81], v212 offset:3072
	s_waitcnt lgkmcnt(1)
	v_mfma_f32_32x32x16_bf16 v[50:65], v[66:69], v[94:97], v[50:65]
	ds_read_b128 v[90:93], v174 offset:33056
	ds_read_b128 v[94:97], v174 offset:33088
	ds_read_b128 v[98:101], v174 offset:33120
	ds_read_b128 v[70:73], v174 offset:33152
	v_mfma_f32_32x32x16_bf16 v[34:49], v[66:69], v[74:77], v[34:49]
	ds_read_b128 v[66:69], v212 offset:4096
	ds_read_b128 v[74:77], v212 offset:5120
	s_waitcnt lgkmcnt(3)
	v_mfma_f32_32x32x16_bf16 v[102:117], v[78:81], v[126:129], v[86:101]
	v_mfma_f32_32x32x16_bf16 v[86:101], v[78:81], v[134:137], v[86:101]
	s_waitcnt lgkmcnt(1)
	v_mfma_f32_32x32x16_bf16 v[86:101], v[66:69], v[146:149], v[86:101]
	v_mfma_f32_32x32x16_bf16 v[102:117], v[66:69], v[122:125], v[102:117]
	ds_read_b128 v[66:69], v212 offset:6144
	s_waitcnt lgkmcnt(1)
	v_mfma_f32_32x32x16_bf16 v[86:101], v[74:77], v[142:145], v[86:101]
	v_mfma_f32_32x32x16_bf16 v[102:117], v[74:77], v[130:133], v[102:117]
	ds_read_b128 v[74:77], v212 offset:15360
	s_waitcnt lgkmcnt(1)
	v_mfma_f32_32x32x16_bf16 v[86:101], v[66:69], v[138:141], v[86:101]
	v_mfma_f32_32x32x16_bf16 v[102:117], v[66:69], v[118:121], v[102:117]
	s_nop 10
	v_cvt_pk_bf16_f32 v78, v86, v87
	v_cvt_pk_bf16_f32 v80, v90, v91
	v_cvt_pk_bf16_f32 v79, v88, v89
	v_cvt_pk_bf16_f32 v81, v92, v93
	ds_read_b128 v[86:89], v212 offset:16384
	ds_read_b128 v[90:93], v212 offset:23552
	v_cvt_pk_bf16_f32 v66, v102, v103
	v_cvt_pk_bf16_f32 v67, v104, v105
	v_cvt_pk_bf16_f32 v68, v106, v107
	v_cvt_pk_bf16_f32 v69, v108, v109
	v_pk_max_i16 v66, v66, 0
	v_pk_max_i16 v67, v67, 0
	v_pk_max_i16 v68, v68, 0
	v_pk_max_i16 v69, v69, 0
	s_nop 1
	v_pk_max_i16 v78, v78, 0
	v_pk_max_i16 v79, v79, 0
	v_pk_max_i16 v80, v80, 0
	v_pk_max_i16 v81, v81, 0
	s_nop 1
	v_cvt_pk_bf16_f32 v94, v94, v95
	s_waitcnt lgkmcnt(2)
	v_mfma_f32_32x32x16_bf16 v[18:33], v[74:77], v[78:81], v[18:33]
	v_cvt_pk_bf16_f32 v95, v96, v97
	v_cvt_pk_bf16_f32 v96, v98, v99
	v_cvt_pk_bf16_f32 v97, v100, v101
	v_pk_max_i16 v94, v94, 0
	v_pk_max_i16 v95, v95, 0
	v_pk_max_i16 v96, v96, 0
	v_pk_max_i16 v97, v97, 0
	s_nop 1
	v_mfma_f32_32x32x16_bf16 v[2:17], v[74:77], v[66:69], v[2:17]
	v_cvt_pk_bf16_f32 v74, v110, v111
	v_cvt_pk_bf16_f32 v75, v112, v113
	v_cvt_pk_bf16_f32 v76, v114, v115
	v_cvt_pk_bf16_f32 v77, v116, v117
	v_pk_max_i16 v74, v74, 0
	v_pk_max_i16 v75, v75, 0
	v_pk_max_i16 v76, v76, 0
	v_pk_max_i16 v77, v77, 0
	s_nop 1
	s_waitcnt lgkmcnt(0)
	v_mfma_f32_32x32x16_bf16 v[50:65], v[90:93], v[66:69], v[50:65]
	ds_read_b128 v[66:69], v212 offset:24576
	v_mfma_f32_32x32x16_bf16 v[34:49], v[90:93], v[78:81], v[34:49]
	ds_read_b128 v[102:105], v212 offset:7168
	v_mfma_f32_32x32x16_bf16 v[2:17], v[86:89], v[74:77], v[2:17]
	s_waitcnt lgkmcnt(1)
	v_mfma_f32_32x32x16_bf16 v[50:65], v[66:69], v[74:77], v[50:65]
	ds_read_b128 v[74:77], v174 offset:33184
	ds_read_b128 v[78:81], v174 offset:33216
	v_mfma_f32_32x32x16_bf16 v[34:49], v[66:69], v[94:97], v[34:49]
	ds_read_b128 v[66:69], v212 offset:8192
	v_mfma_f32_32x32x16_bf16 v[18:33], v[86:89], v[94:97], v[18:33]
	s_waitcnt lgkmcnt(1)
	v_mfma_f32_32x32x16_bf16 v[86:101], v[102:105], v[126:129], v[70:85]
	v_mfma_f32_32x32x16_bf16 v[70:85], v[102:105], v[134:137], v[70:85]
	ds_read_b128 v[102:105], v212 offset:9216
	v_lshlrev_b32_e32 v135, 2, v1
	v_add_u32_e32 v134, v172, v174
	s_waitcnt lgkmcnt(1)
	v_mfma_f32_32x32x16_bf16 v[86:101], v[66:69], v[122:125], v[86:101]
	v_mfma_f32_32x32x16_bf16 v[70:85], v[66:69], v[146:149], v[70:85]
	ds_read_b128 v[66:69], v212 offset:10240
	s_waitcnt lgkmcnt(1)
	v_mfma_f32_32x32x16_bf16 v[86:101], v[102:105], v[130:133], v[86:101]
	v_mfma_f32_32x32x16_bf16 v[70:85], v[102:105], v[142:145], v[70:85]
	ds_read_b128 v[102:105], v212 offset:17408
	s_waitcnt lgkmcnt(1)
	v_mfma_f32_32x32x16_bf16 v[86:101], v[66:69], v[118:121], v[86:101]
	v_mfma_f32_32x32x16_bf16 v[70:85], v[66:69], v[138:141], v[70:85]
	s_nop 10
	v_cvt_pk_bf16_f32 v68, v90, v91
	v_cvt_pk_bf16_f32 v69, v92, v93
	ds_read_b128 v[90:93], v212 offset:25600
	v_cvt_pk_bf16_f32 v66, v86, v87
	v_cvt_pk_bf16_f32 v67, v88, v89
	v_pk_max_i16 v66, v66, 0
	v_pk_max_i16 v67, v67, 0
	v_pk_max_i16 v68, v68, 0
	v_pk_max_i16 v69, v69, 0
	s_nop 1
	v_cvt_pk_bf16_f32 v70, v70, v71
	v_cvt_pk_bf16_f32 v71, v72, v73
	s_waitcnt lgkmcnt(1)
	v_mfma_f32_32x32x16_bf16 v[2:17], v[102:105], v[66:69], v[2:17]
	v_cvt_pk_bf16_f32 v72, v74, v75
	v_cvt_pk_bf16_f32 v73, v76, v77
	ds_read_b128 v[74:77], v212 offset:18432
	v_cvt_pk_bf16_f32 v86, v94, v95
	v_cvt_pk_bf16_f32 v87, v96, v97
	v_cvt_pk_bf16_f32 v88, v98, v99
	s_waitcnt lgkmcnt(1)
	v_mfma_f32_32x32x16_bf16 v[50:65], v[90:93], v[66:69], v[50:65]
	ds_read_b128 v[66:69], v212 offset:26624
	v_cvt_pk_bf16_f32 v89, v100, v101
	v_pk_max_i16 v86, v86, 0
	v_pk_max_i16 v87, v87, 0
	v_pk_max_i16 v88, v88, 0
	v_pk_max_i16 v89, v89, 0
	s_nop 1
	v_pk_max_i16 v70, v70, 0
	v_pk_max_i16 v71, v71, 0
	v_pk_max_i16 v72, v72, 0
	v_pk_max_i16 v73, v73, 0
	s_nop 1
	v_cvt_pk_bf16_f32 v78, v78, v79
	v_cvt_pk_bf16_f32 v79, v80, v81
	s_waitcnt lgkmcnt(1)
	v_mfma_f32_32x32x16_bf16 v[2:17], v[74:77], v[86:89], v[2:17]
	v_cvt_pk_bf16_f32 v80, v82, v83
	v_cvt_pk_bf16_f32 v81, v84, v85
	v_pk_max_i16 v78, v78, 0
	v_pk_max_i16 v79, v79, 0
	v_pk_max_i16 v80, v80, 0
	v_pk_max_i16 v81, v81, 0
	s_nop 1
	s_waitcnt lgkmcnt(0)
	v_mfma_f32_32x32x16_bf16 v[50:65], v[66:69], v[86:89], v[50:65]
	v_mfma_f32_32x32x16_bf16 v[34:49], v[90:93], v[70:73], v[34:49]
	s_nop 10
	v_add_f32_e64 v130, v10, v58
	v_add_f32_e64 v131, v11, v59
	v_add_f32_e64 v132, v12, v60
	v_add_f32_e64 v133, v13, v61
	v_add_f32_e64 v138, v4, v52
	v_add_f32_e64 v139, v5, v53
	v_pk_add_f32 v[140:141], v[16:17], v[64:65]
	v_pk_add_f32 v[142:143], v[8:9], v[56:57]
	v_pk_add_f32 v[144:145], v[14:15], v[62:63]
	v_pk_add_f32 v[146:147], v[6:7], v[54:55]
	v_mfma_f32_32x32x16_bf16 v[18:33], v[102:105], v[70:73], v[18:33]
	ds_read2st64_b32 v[70:71], v135 offset0:133 offset1:134
	v_add_f32_e64 v148, v2, v50
	v_add_f32_e64 v149, v3, v51
	v_add_f32_e64 v144, v146, v144
	v_add_f32_e64 v145, v147, v145
	v_pk_add_f32 v[140:141], v[142:143], v[140:141]
	v_pk_add_f32 v[132:133], v[138:139], v[132:133]
	v_pk_add_f32 v[130:131], v[148:149], v[130:131]
	v_pk_add_f32 v[132:133], v[132:133], v[140:141]
	v_pk_add_f32 v[130:131], v[130:131], v[144:145]
	v_mfma_f32_32x32x16_bf16 v[34:49], v[66:69], v[78:81], v[34:49]
	v_pk_mov_b32 v[138:139], v[130:131], v[132:133] op_sel:[1,0]
	v_mov_b32_e32 v131, v133
	s_waitcnt vmcnt(0) lgkmcnt(0)
	v_mul_f32_e32 v66, v175, v70
	v_pk_add_f32 v[130:131], v[138:139], v[130:131]
	ds_write_b32 v173, v66 offset:512
	v_mul_f32_e32 v66, v175, v71
	v_pk_add_f32 v[130:131], v[130:131], v[130:131] op_sel:[0,1] op_sel_hi:[1,0]
	s_waitcnt lgkmcnt(0)
	ds_read_b128 v[102:105], v174 offset:34560
	ds_read_b128 v[98:101], v174 offset:34592
	ds_read_b128 v[110:113], v174 offset:34624
	ds_read_b128 v[106:109], v174 offset:34656
	ds_read_b128 v[114:117], v174 offset:34688
	ds_read_b128 v[122:125], v174 offset:34720
	ds_read_b128 v[118:121], v174 offset:34752
	ds_read_b128 v[126:129], v174 offset:34784
	v_mov_b32_dpp v66, v66 quad_perm:[1,0,3,2] row_mask:0xf bank_mask:0xf bound_ctrl:1
	v_mov_b32_e32 v131, v130
	v_fmac_f32_e32 v66, v175, v71
	s_nop 0
	v_permlane32_swap_b32_e32 v130, v131
	v_add_f32_dpp v66, v66, v66 quad_perm:[2,3,0,1] row_mask:0xf bank_mask:0xf bound_ctrl:1
	v_add_f32_e32 v130, v130, v131
	v_fmamk_f32 v65, v130, 0xbc800000, v65
	v_add_f32_dpp v66, v66, v66 row_half_mirror row_mask:0xf bank_mask:0xf bound_ctrl:1
	v_fmamk_f32 v64, v130, 0xbc800000, v64
	v_fmamk_f32 v63, v130, 0xbc800000, v63
	v_fmamk_f32 v62, v130, 0xbc800000, v62
	v_fmamk_f32 v61, v130, 0xbc800000, v61
	v_fmamk_f32 v60, v130, 0xbc800000, v60
	v_fmamk_f32 v59, v130, 0xbc800000, v59
	v_fmamk_f32 v58, v130, 0xbc800000, v58
	v_fmamk_f32 v57, v130, 0xbc800000, v57
	v_fmamk_f32 v56, v130, 0xbc800000, v56
	v_fmamk_f32 v55, v130, 0xbc800000, v55
	v_fmamk_f32 v54, v130, 0xbc800000, v54
	v_fmamk_f32 v53, v130, 0xbc800000, v53
	v_fmamk_f32 v52, v130, 0xbc800000, v52
	v_fmamk_f32 v51, v130, 0xbc800000, v51
	v_fmac_f32_e32 v50, 0xbc800000, v130
	v_add_f32_dpp v66, v66, v66 row_ror:8 row_mask:0xf bank_mask:0xf bound_ctrl:1
	v_fmamk_f32 v17, v130, 0xbc800000, v17
	v_fmamk_f32 v16, v130, 0xbc800000, v16
	v_fmamk_f32 v15, v130, 0xbc800000, v15
	v_fmamk_f32 v14, v130, 0xbc800000, v14
	v_fmamk_f32 v13, v130, 0xbc800000, v13
	v_fmamk_f32 v12, v130, 0xbc800000, v12
	v_fmamk_f32 v11, v130, 0xbc800000, v11
	v_fmamk_f32 v10, v130, 0xbc800000, v10
	v_fmamk_f32 v9, v130, 0xbc800000, v9
	v_fmamk_f32 v8, v130, 0xbc800000, v8
	v_fmamk_f32 v7, v130, 0xbc800000, v7
	v_fmamk_f32 v6, v130, 0xbc800000, v6
	v_fmamk_f32 v5, v130, 0xbc800000, v5
	v_fmamk_f32 v4, v130, 0xbc800000, v4
	v_fmamk_f32 v3, v130, 0xbc800000, v3
	v_fmac_f32_e32 v2, 0xbc800000, v130
	v_pk_mul_f32 v[130:131], v[54:55], v[54:55]
	v_pk_mul_f32 v[132:133], v[62:63], v[62:63]
	v_pk_mul_f32 v[138:139], v[50:51], v[50:51]
	v_pk_mul_f32 v[140:141], v[58:59], v[58:59]
	v_pk_mul_f32 v[142:143], v[56:57], v[56:57]
	v_pk_mul_f32 v[144:145], v[64:65], v[64:65]
	v_pk_mul_f32 v[146:147], v[52:53], v[52:53]
	v_pk_mul_f32 v[148:149], v[60:61], v[60:61]
	v_mov_b32_e32 v67, v66
	v_pk_fma_f32 v[148:149], v[12:13], v[12:13], v[148:149]
	v_pk_fma_f32 v[146:147], v[4:5], v[4:5], v[146:147]
	v_pk_fma_f32 v[144:145], v[16:17], v[16:17], v[144:145]
	v_pk_fma_f32 v[142:143], v[8:9], v[8:9], v[142:143]
	v_pk_fma_f32 v[140:141], v[10:11], v[10:11], v[140:141]
	v_pk_fma_f32 v[138:139], v[2:3], v[2:3], v[138:139]
	v_pk_fma_f32 v[132:133], v[14:15], v[14:15], v[132:133]
	v_pk_fma_f32 v[130:131], v[6:7], v[6:7], v[130:131]
	v_permlane16_swap_b32_e32 v66, v67
	v_pk_add_f32 v[130:131], v[130:131], v[132:133]
	v_pk_add_f32 v[132:133], v[138:139], v[140:141]
	v_pk_add_f32 v[138:139], v[142:143], v[144:145]
	v_pk_add_f32 v[140:141], v[146:147], v[148:149]
	v_mfma_f32_32x32x16_bf16 v[18:33], v[74:77], v[78:81], v[18:33]
	v_add_f32_e32 v136, v66, v67
	ds_read_b128 v[70:73], v134 offset:512
	ds_read_b128 v[66:69], v134 offset:544
	ds_read_b128 v[78:81], v134 offset:576
	ds_read_b128 v[74:77], v134 offset:608
	ds_read_b128 v[82:85], v134 offset:640
	ds_read_b128 v[90:93], v134 offset:672
	ds_read_b128 v[86:89], v134 offset:704
	ds_read_b128 v[94:97], v134 offset:736
	v_pk_add_f32 v[138:139], v[140:141], v[138:139]
	v_pk_add_f32 v[130:131], v[132:133], v[130:131]
	s_waitcnt lgkmcnt(8)
	v_pk_mul_f32 v[140:141], v[126:127], v[62:63]
	v_pk_mov_b32 v[132:133], v[130:131], v[138:139] op_sel:[1,0]
	v_mov_b32_e32 v131, v139
	v_pk_mul_f32 v[138:139], v[122:123], v[54:55]
	v_pk_mul_f32 v[142:143], v[114:115], v[50:51]
	v_pk_mul_f32 v[144:145], v[118:119], v[58:59]
	v_pk_mul_f32 v[146:147], v[124:125], v[56:57]
	v_pk_mul_f32 v[148:149], v[128:129], v[64:65]
	v_pk_mul_f32 v[154:155], v[116:117], v[52:53]
	v_pk_mul_f32 v[156:157], v[120:121], v[60:61]
	v_pk_fma_f32 v[154:155], v[104:105], v[4:5], v[154:155]
	v_pk_fma_f32 v[156:157], v[112:113], v[12:13], v[156:157]
	v_pk_fma_f32 v[148:149], v[108:109], v[16:17], v[148:149]
	v_pk_fma_f32 v[146:147], v[100:101], v[8:9], v[146:147]
	v_pk_fma_f32 v[144:145], v[110:111], v[10:11], v[144:145]
	v_pk_fma_f32 v[142:143], v[102:103], v[2:3], v[142:143]
	v_pk_fma_f32 v[140:141], v[106:107], v[14:15], v[140:141]
	v_pk_fma_f32 v[138:139], v[98:99], v[6:7], v[138:139]
	v_pk_add_f32 v[130:131], v[132:133], v[130:131]
	v_pk_add_f32 v[138:139], v[138:139], v[140:141]
	v_pk_add_f32 v[140:141], v[142:143], v[144:145]
	v_pk_add_f32 v[142:143], v[146:147], v[148:149]
	v_pk_add_f32 v[144:145], v[154:155], v[156:157]
	v_pk_add_f32 v[132:133], v[130:131], v[130:131] op_sel:[0,1] op_sel_hi:[1,0]
	v_pk_add_f32 v[142:143], v[144:145], v[142:143]
	v_pk_add_f32 v[138:139], v[140:141], v[138:139]
	v_add_f32_e32 v133, v142, v143
	v_add_f32_e32 v130, v138, v139
	s_waitcnt lgkmcnt(2)
	v_pk_mul_f32 v[138:139], v[90:91], v[54:55]
	s_waitcnt lgkmcnt(0)
	v_pk_mul_f32 v[140:141], v[94:95], v[62:63]
	v_pk_mul_f32 v[142:143], v[82:83], v[50:51]
	v_pk_mul_f32 v[144:145], v[86:87], v[58:59]
	v_pk_mul_f32 v[146:147], v[92:93], v[56:57]
	v_pk_mul_f32 v[148:149], v[96:97], v[64:65]
	v_pk_mul_f32 v[154:155], v[84:85], v[52:53]
	v_pk_mul_f32 v[156:157], v[88:89], v[60:61]
	v_add_f32_e32 v130, v130, v133
	v_pk_fma_f32 v[156:157], v[80:81], v[12:13], v[156:157]
	v_pk_fma_f32 v[154:155], v[72:73], v[4:5], v[154:155]
	v_pk_fma_f32 v[148:149], v[76:77], v[16:17], v[148:149]
	v_pk_fma_f32 v[146:147], v[68:69], v[8:9], v[146:147]
	v_pk_fma_f32 v[144:145], v[78:79], v[10:11], v[144:145]
	v_pk_fma_f32 v[142:143], v[70:71], v[2:3], v[142:143]
	v_pk_fma_f32 v[140:141], v[74:75], v[14:15], v[140:141]
	v_pk_fma_f32 v[138:139], v[66:67], v[6:7], v[138:139]
	v_mov_b32_e32 v133, v130
	v_pk_add_f32 v[138:139], v[138:139], v[140:141]
	v_pk_add_f32 v[140:141], v[142:143], v[144:145]
	v_pk_add_f32 v[142:143], v[146:147], v[148:149]
	v_pk_add_f32 v[144:145], v[154:155], v[156:157]
	v_permlane32_swap_b32_e32 v130, v133
	v_pk_add_f32 v[142:143], v[144:145], v[142:143]
	v_add_f32_e32 v160, v130, v133
	v_pk_add_f32 v[138:139], v[140:141], v[138:139]
	v_add_f32_e32 v133, v142, v143
	v_pk_add_f32 v[140:141], v[26:27], v[42:43]
	v_pk_add_f32 v[142:143], v[28:29], v[44:45]
	v_pk_add_f32 v[144:145], v[20:21], v[36:37]
	v_pk_add_f32 v[146:147], v[32:33], v[48:49]
	v_pk_add_f32 v[148:149], v[24:25], v[40:41]
	v_pk_add_f32 v[154:155], v[30:31], v[46:47]
	v_pk_add_f32 v[156:157], v[22:23], v[38:39]
	v_pk_add_f32 v[158:159], v[18:19], v[34:35]
	v_pk_add_f32 v[154:155], v[156:157], v[154:155]
	v_pk_add_f32 v[146:147], v[148:149], v[146:147]
	v_pk_add_f32 v[142:143], v[144:145], v[142:143]
	v_pk_add_f32 v[140:141], v[158:159], v[140:141]
	v_pk_add_f32 v[142:143], v[142:143], v[146:147]
	v_pk_add_f32 v[140:141], v[140:141], v[154:155]
	v_add_f32_e32 v130, v138, v139
	v_pk_mov_b32 v[144:145], v[140:141], v[142:143] op_sel:[1,0]
	v_mov_b32_e32 v141, v143
	v_pk_add_f32 v[140:141], v[144:145], v[140:141]
	v_add_f32_e32 v133, v130, v133
	v_pk_add_f32 v[140:141], v[140:141], v[140:141] op_sel:[0,1] op_sel_hi:[1,0]
	v_mov_b32_e32 v131, v132
	v_mov_b32_e32 v130, v140
	s_nop 1
	v_permlane32_swap_b32_e32 v140, v130
	v_add_f32_e32 v130, v140, v130
	v_fmamk_f32 v49, v130, 0xbc800000, v49
	v_fmamk_f32 v48, v130, 0xbc800000, v48
	v_fmamk_f32 v47, v130, 0xbc800000, v47
	v_fmamk_f32 v46, v130, 0xbc800000, v46
	v_fmamk_f32 v45, v130, 0xbc800000, v45
	v_fmamk_f32 v44, v130, 0xbc800000, v44
	v_fmamk_f32 v43, v130, 0xbc800000, v43
	v_fmamk_f32 v42, v130, 0xbc800000, v42
	v_fmamk_f32 v41, v130, 0xbc800000, v41
	v_fmamk_f32 v40, v130, 0xbc800000, v40
	v_fmamk_f32 v39, v130, 0xbc800000, v39
	v_fmamk_f32 v38, v130, 0xbc800000, v38
	v_fmamk_f32 v37, v130, 0xbc800000, v37
	v_fmamk_f32 v36, v130, 0xbc800000, v36
	v_fmamk_f32 v35, v130, 0xbc800000, v35
	v_fmac_f32_e32 v34, 0xbc800000, v130
	v_fmamk_f32 v33, v130, 0xbc800000, v33
	v_fmamk_f32 v32, v130, 0xbc800000, v32
	v_fmamk_f32 v31, v130, 0xbc800000, v31
	v_fmamk_f32 v30, v130, 0xbc800000, v30
	v_fmamk_f32 v29, v130, 0xbc800000, v29
	v_fmamk_f32 v28, v130, 0xbc800000, v28
	v_fmamk_f32 v27, v130, 0xbc800000, v27
	v_fmamk_f32 v26, v130, 0xbc800000, v26
	v_fmamk_f32 v25, v130, 0xbc800000, v25
	v_fmamk_f32 v24, v130, 0xbc800000, v24
	v_fmamk_f32 v23, v130, 0xbc800000, v23
	v_fmamk_f32 v22, v130, 0xbc800000, v22
	v_fmamk_f32 v21, v130, 0xbc800000, v21
	v_fmamk_f32 v20, v130, 0xbc800000, v20
	v_fmamk_f32 v19, v130, 0xbc800000, v19
	v_fmac_f32_e32 v18, 0xbc800000, v130
	v_pk_mul_f32 v[140:141], v[38:39], v[38:39]
	v_pk_mul_f32 v[142:143], v[46:47], v[46:47]
	v_pk_mul_f32 v[144:145], v[34:35], v[34:35]
	v_pk_mul_f32 v[146:147], v[42:43], v[42:43]
	v_pk_mul_f32 v[148:149], v[40:41], v[40:41]
	v_pk_mul_f32 v[154:155], v[48:49], v[48:49]
	v_pk_mul_f32 v[156:157], v[36:37], v[36:37]
	v_pk_mul_f32 v[158:159], v[44:45], v[44:45]
	v_pk_fma_f32 v[156:157], v[20:21], v[20:21], v[156:157]
	v_pk_fma_f32 v[158:159], v[28:29], v[28:29], v[158:159]
	v_pk_fma_f32 v[154:155], v[32:33], v[32:33], v[154:155]
	v_pk_fma_f32 v[148:149], v[24:25], v[24:25], v[148:149]
	v_pk_fma_f32 v[146:147], v[26:27], v[26:27], v[146:147]
	v_pk_fma_f32 v[144:145], v[18:19], v[18:19], v[144:145]
	v_pk_fma_f32 v[142:143], v[30:31], v[30:31], v[142:143]
	v_pk_fma_f32 v[140:141], v[22:23], v[22:23], v[140:141]
	v_permlane32_swap_b32_e32 v132, v131
	v_pk_add_f32 v[140:141], v[140:141], v[142:143]
	v_pk_add_f32 v[142:143], v[144:145], v[146:147]
	v_pk_add_f32 v[144:145], v[148:149], v[154:155]
	v_pk_add_f32 v[146:147], v[156:157], v[158:159]
	v_pk_add_f32 v[140:141], v[142:143], v[140:141]
	v_pk_add_f32 v[144:145], v[146:147], v[144:145]
	v_pk_mul_f32 v[122:123], v[122:123], v[38:39]
	v_pk_mov_b32 v[142:143], v[140:141], v[144:145] op_sel:[1,0]
	v_mov_b32_e32 v141, v145
	v_pk_add_f32 v[140:141], v[142:143], v[140:141]
	v_pk_mul_f32 v[126:127], v[126:127], v[46:47]
	v_pk_add_f32 v[140:141], v[140:141], v[140:141] op_sel:[0,1] op_sel_hi:[1,0]
	v_pk_mul_f32 v[114:115], v[114:115], v[34:35]
	v_mov_b32_e32 v130, v140
	s_nop 1
	v_permlane32_swap_b32_e32 v140, v130
	v_mov_b32_e32 v141, v132
	v_pk_add_f32 v[130:131], v[140:141], v[130:131]
	v_pk_mul_f32 v[118:119], v[118:119], v[42:43]
	v_pk_fma_f32 v[130:131], v[130:131], s[0:1], v[152:153] op_sel_hi:[1,0,0]
	v_pk_mul_f32 v[124:125], v[124:125], v[40:41]
	v_mul_f32_e32 v132, 0x4b800000, v131
	v_cmp_gt_f32_e32 vcc, s1, v131
	v_pk_mul_f32 v[128:129], v[128:129], v[48:49]
	v_pk_mul_f32 v[116:117], v[116:117], v[36:37]
	v_pk_mul_f32 v[120:121], v[120:121], v[44:45]
	v_cndmask_b32_e32 v131, v131, v132, vcc
	v_mul_f32_e32 v132, 0x4b800000, v130
	v_cmp_gt_f32_e64 s[0:1], s1, v130
	v_pk_fma_f32 v[112:113], v[112:113], v[28:29], v[120:121]
	v_pk_fma_f32 v[104:105], v[104:105], v[20:21], v[116:117]
	v_pk_fma_f32 v[108:109], v[108:109], v[32:33], v[128:129]
	v_pk_fma_f32 v[100:101], v[100:101], v[24:25], v[124:125]
	v_pk_fma_f32 v[110:111], v[110:111], v[26:27], v[118:119]
	v_pk_fma_f32 v[102:103], v[102:103], v[18:19], v[114:115]
	v_pk_fma_f32 v[106:107], v[106:107], v[30:31], v[126:127]
	v_pk_fma_f32 v[98:99], v[98:99], v[22:23], v[122:123]
	v_rsq_f32_e32 v131, v131
	v_cndmask_b32_e64 v130, v130, v132, s[0:1]
	v_pk_add_f32 v[98:99], v[98:99], v[106:107]
	v_pk_add_f32 v[102:103], v[102:103], v[110:111]
	v_pk_add_f32 v[100:101], v[100:101], v[108:109]
	v_pk_add_f32 v[104:105], v[104:105], v[112:113]
	v_rsq_f32_e32 v132, v130
	v_pk_add_f32 v[100:101], v[104:105], v[100:101]
	v_pk_add_f32 v[98:99], v[102:103], v[98:99]
	v_mul_f32_e32 v130, 0x45800000, v131
	v_add_f32_e32 v98, v98, v99
	v_add_f32_e32 v99, v100, v101
	v_add_f32_e32 v98, v98, v99
	v_mov_b32_e32 v99, v98
	v_pk_mul_f32 v[90:91], v[90:91], v[38:39]
	v_pk_mul_f32 v[94:95], v[94:95], v[46:47]
	v_pk_mul_f32 v[82:83], v[82:83], v[34:35]
	v_pk_mul_f32 v[86:87], v[86:87], v[42:43]
	v_cndmask_b32_e32 v130, v131, v130, vcc
	v_mul_f32_e32 v131, 0x45800000, v132
	v_permlane32_swap_b32_e32 v98, v99
	v_pk_fma_f32 v[78:79], v[78:79], v[26:27], v[86:87]
	v_pk_fma_f32 v[70:71], v[70:71], v[18:19], v[82:83]
	v_pk_fma_f32 v[74:75], v[74:75], v[30:31], v[94:95]
	v_pk_fma_f32 v[66:67], v[66:67], v[22:23], v[90:91]
	v_cndmask_b32_e64 v131, v132, v131, s[0:1]
	v_add_f32_e32 v98, v98, v99
	v_pk_add_f32 v[66:67], v[66:67], v[74:75]
	v_pk_add_f32 v[70:71], v[70:71], v[78:79]
	v_mul_f32_e32 v139, v160, v130
	v_mul_f32_e32 v98, v98, v131
	v_pk_add_f32 v[66:67], v[70:71], v[66:67]
	v_cmp_gt_u32_e32 vcc, 32, v1
	v_add_f32_e32 v66, v66, v67
	v_pk_mul_f32 v[92:93], v[92:93], v[40:41]
	v_cndmask_b32_e32 v67, v98, v139, vcc
	v_add_f32_e32 v67, s12, v67
	v_pk_mul_f32 v[96:97], v[96:97], v[48:49]
	v_pk_mul_f32 v[84:85], v[84:85], v[36:37]
	v_pk_mul_f32 v[88:89], v[88:89], v[44:45]
	v_mul_f32_e32 v67, 0xbfb8aa3b, v67
	v_pk_fma_f32 v[80:81], v[80:81], v[28:29], v[88:89]
	v_pk_fma_f32 v[72:73], v[72:73], v[20:21], v[84:85]
	v_pk_fma_f32 v[76:77], v[76:77], v[32:33], v[96:97]
	v_pk_fma_f32 v[68:69], v[68:69], v[24:25], v[92:93]
	v_exp_f32_e32 v70, v67
	v_pk_add_f32 v[68:69], v[68:69], v[76:77]
	v_pk_add_f32 v[72:73], v[72:73], v[80:81]
	v_cmp_lt_i32_e64 s[0:1], 0, v151
	v_pk_add_f32 v[68:69], v[72:73], v[68:69]
	v_mov_b32_e32 v137, v136
	v_add_f32_e32 v67, v68, v69
	v_add_f32_e32 v67, v66, v67
	v_add_f32_e32 v66, 1.0, v70
	v_rcp_f32_e32 v66, v66
	v_mov_b32_e32 v69, 0xff800000
	v_mov_b32_e32 v138, v133
	v_mov_b32_e32 v68, v67
	v_cndmask_b32_e64 v70, v69, v66, s[0:1]
	v_mbcnt_lo_u32_b32 v66, -1, 0
	v_mbcnt_hi_u32_b32 v66, -1, v66
	v_permlane32_swap_b32_e32 v136, v137
	v_permlane32_swap_b32_e32 v133, v138
	v_permlane32_swap_b32_e32 v67, v68
	v_and_b32_e32 v86, 64, v66
	v_mov_b32_e32 v71, 8
	v_mov_b32_e32 v66, 0
